# in_proj and out_proj K-loops also wait per phase with counted vmcnt(10)
# speedup vs baseline: 1.0420x; 1.0012x over previous
; #define G_WAIT_V(n) asm volatile("s_waitcnt vmcnt(" #n ")" ::: "memory")
; #define G_WAIT_L(n) asm volatile("s_waitcnt lgkmcnt(" #n ")" ::: "memory")
; #define G_BAR do { asm volatile("" ::: "memory"); __builtin_amdgcn_s_barrier(); asm volatile("" ::: "memory"); } while (0)
; #define G_SCHED __builtin_amdgcn_sched_barrier(0)
; #define STG_A(b, h, kt) do { const unsigned char* _g = A + (size_t)KT_(kt) * ASTEP; \
;         dma16((const void*)(_g + (size_t)((h) * 128) * ROWB), ROWB ? aoff[0][0] : aoff[h][0], lds_u + SA_(b, h) + dma0); \
;         dma16((const void*)(_g + (size_t)((h) * 128 + 64) * ROWB), ROWB ? aoff[0][0] : aoff[h][1], lds_u + SA_(b, h) + dma1); } while (0)
; #define STG_B(b, h, kt) do { const unsigned char* _g = img + (size_t)KT_(kt) * 32768 + (h) * 16384; \
;         dma16((const void*)(_g + dma0), boffl, lds_u + SB_(b, h) + dma0); \
;         dma16((const void*)(_g + dma1), boffl, lds_u + SB_(b, h) + dma1); } while (0)
; #define LDA_(dst, b, h) do { _Pragma("unroll") for (int _m = 0; _m < 4; ++_m) { \
;         dst[_m].lo = *(LAS3 const i32x4d*)(ap0 + SA_(b, h) + _m * 2048); \
;         dst[_m].hi = *(LAS3 const i32x4d*)(ap1 + SA_(b, h) + _m * 2048); } } while (0)
; #define LDBF(dst, b, h) do { _Pragma("unroll") for (int _n = 0; _n < 2; ++_n) { \
;         dst[_n].lo = *(LAS3 const i32x4d*)(bp0 + (SB_(b, h) - 4 * GHTB) + _n * 8192); \
;         dst[_n].hi = *(LAS3 const i32x4d*)(bp1 + (SB_(b, h) - 4 * GHTB) + _n * 8192); } } while (0)
;     ...
;     for (int t = 0; t < nt; t += 2) {
;         const int t1 = (t + 1 < nt) ? t + 1 : nt - 1, t2 = (t + 2 < nt) ? t + 2 : nt - 1, t3 = (t + 3 < nt) ? t + 3 : nt - 1;
;         LDBF(B0, 0, 0); G_SCHED; LDA_(At, 0, 0); STG_A(1, 1, t1);
;         G_WAIT_L(8); G_BAR; G_WAIT_L(0); MMAD(0, 0, At, B0); G_BAR; G_SCHED;
;         LDBF(B1, 0, 1); STG_B(0, 0, t2);
;         G_BAR; G_WAIT_L(0); MMAD(0, 1, At, B1); G_BAR;
;         LDA_(At, 0, 1); STG_A(0, 0, t2);
;         G_BAR; G_WAIT_L(0); MMAD(1, 0, At, B0); G_BAR; G_SCHED;
;         STG_B(0, 1, t2);
;         G_WAIT_V(6); G_BAR; MMAD(1, 1, At, B1); G_BAR;
.LBB0_90:
	ds_read_b128 v[136:139], v133
	ds_read_b128 v[140:143], v133 offset:8192
	ds_read_b128 v[144:147], v134
	ds_read_b128 v[148:151], v134 offset:8192
	s_add_i32 s1, s0, -1
	s_add_i32 s8, s0, -2
	s_min_u32 s68, s1, vcc_hi
	s_min_u32 s8, s8, vcc_hi
	s_add_i32 s8, s8, vcc_lo
	s_lshl_b32 s8, s8, 7
	s_and_b32 s8, s8, 0xf80
	ds_read_b128 v[152:155], v131
	ds_read_b128 v[156:159], v131 offset:2048
	ds_read_b128 v[160:163], v132
	ds_read_b128 v[164:167], v132 offset:2048
	ds_read_b128 v[168:171], v131 offset:4096
	ds_read_b128 v[172:175], v131 offset:6144
	ds_read_b128 v[176:179], v132 offset:4096
	ds_read_b128 v[180:183], v132 offset:6144
	s_add_u32 s69, s54, s8
	s_addc_u32 s70, s55, 0
	s_add_u32 s8, s69, 0x80000
	s_addc_u32 s9, s70, 0
	s_mov_b32 s71, m0
	s_mov_b32 m0, s31
	s_nop 2
	global_load_lds_dwordx4 v128, s[8:9]
	s_mov_b32 m0, s71
	s_add_u32 s8, s69, 0xc0000
	s_addc_u32 s9, s70, 0
	s_mov_b32 s69, m0
	s_mov_b32 m0, s33
	s_nop 2
	global_load_lds_dwordx4 v128, s[8:9]
	s_mov_b32 m0, s69
	s_waitcnt lgkmcnt(8)
	s_waitcnt vmcnt(10)
	s_barrier
	s_waitcnt lgkmcnt(0)
	s_setprio 1
	s_waitcnt lgkmcnt(7)
	v_mfma_f32_16x16x32_bf16 v[124:127], v[136:139], v[152:155], v[124:127]
	v_mfma_f32_16x16x32_bf16 v[120:123], v[140:143], v[152:155], v[120:123]
	s_waitcnt lgkmcnt(6)
	v_mfma_f32_16x16x32_bf16 v[116:119], v[136:139], v[156:159], v[116:119]
	v_mfma_f32_16x16x32_bf16 v[108:111], v[140:143], v[156:159], v[108:111]
	s_waitcnt lgkmcnt(3)
	v_mfma_f32_16x16x32_bf16 v[100:103], v[136:139], v[168:171], v[100:103]
	v_mfma_f32_16x16x32_bf16 v[92:95], v[140:143], v[168:171], v[92:95]
	s_waitcnt lgkmcnt(2)
	v_mfma_f32_16x16x32_bf16 v[84:87], v[136:139], v[172:175], v[84:87]
	v_mfma_f32_16x16x32_bf16 v[76:79], v[140:143], v[172:175], v[76:79]
	v_mfma_f32_16x16x32_bf16 v[124:127], v[144:147], v[160:163], v[124:127]
	v_mfma_f32_16x16x32_bf16 v[120:123], v[148:151], v[160:163], v[120:123]
	v_mfma_f32_16x16x32_bf16 v[116:119], v[144:147], v[164:167], v[116:119]
	v_mfma_f32_16x16x32_bf16 v[108:111], v[148:151], v[164:167], v[108:111]
	s_waitcnt lgkmcnt(1)
	v_mfma_f32_16x16x32_bf16 v[100:103], v[144:147], v[176:179], v[100:103]
	v_mfma_f32_16x16x32_bf16 v[92:95], v[148:151], v[176:179], v[92:95]
	s_waitcnt lgkmcnt(0)
	v_mfma_f32_16x16x32_bf16 v[84:87], v[144:147], v[180:183], v[84:87]
	v_mfma_f32_16x16x32_bf16 v[76:79], v[148:151], v[180:183], v[76:79]
	s_setprio 0
	s_barrier
	s_add_i32 s68, s68, vcc_lo
	s_and_b32 s68, s68, 31
	s_lshl_b32 s8, s68, 15
	s_add_u32 s70, s5, s8
	s_addc_u32 s71, s89, 0
	s_add_u32 s8, s70, s13
	ds_read_b128 v[184:187], v133 offset:16384
	ds_read_b128 v[188:191], v133 offset:24576
	ds_read_b128 v[192:195], v134 offset:16384
	ds_read_b128 v[196:199], v134 offset:24576
	s_addc_u32 s9, s71, s15
	s_mov_b32 s69, m0
	s_mov_b32 m0, s17
	s_nop 2
	global_load_lds_dwordx4 v135, s[8:9]
	s_mov_b32 m0, s69
	s_add_u32 s8, s70, s14
	s_addc_u32 s9, s71, s18
	s_mov_b32 s69, m0
	s_mov_b32 m0, s19
	s_nop 2
	global_load_lds_dwordx4 v135, s[8:9]
	s_mov_b32 m0, s69
	s_waitcnt vmcnt(10)
	s_barrier
	s_waitcnt lgkmcnt(0)
	s_setprio 1
	s_waitcnt lgkmcnt(3)
	v_mfma_f32_16x16x32_bf16 v[112:115], v[184:187], v[152:155], v[112:115]
	s_waitcnt lgkmcnt(2)
	v_mfma_f32_16x16x32_bf16 v[104:107], v[188:191], v[152:155], v[104:107]
	v_mfma_f32_16x16x32_bf16 v[96:99], v[184:187], v[156:159], v[96:99]
	v_mfma_f32_16x16x32_bf16 v[88:91], v[188:191], v[156:159], v[88:91]
	v_mfma_f32_16x16x32_bf16 v[80:83], v[184:187], v[168:171], v[80:83]
	v_mfma_f32_16x16x32_bf16 v[72:75], v[188:191], v[168:171], v[72:75]
	v_mfma_f32_16x16x32_bf16 v[68:71], v[184:187], v[172:175], v[68:71]
	v_mfma_f32_16x16x32_bf16 v[64:67], v[188:191], v[172:175], v[64:67]
	s_waitcnt lgkmcnt(1)
	v_mfma_f32_16x16x32_bf16 v[112:115], v[192:195], v[160:163], v[112:115]
	s_waitcnt lgkmcnt(0)
	v_mfma_f32_16x16x32_bf16 v[104:107], v[196:199], v[160:163], v[104:107]
	v_mfma_f32_16x16x32_bf16 v[96:99], v[192:195], v[164:167], v[96:99]
	v_mfma_f32_16x16x32_bf16 v[88:91], v[196:199], v[164:167], v[88:91]
	v_mfma_f32_16x16x32_bf16 v[80:83], v[192:195], v[176:179], v[80:83]
	v_mfma_f32_16x16x32_bf16 v[72:75], v[196:199], v[176:179], v[72:75]
	v_mfma_f32_16x16x32_bf16 v[68:71], v[192:195], v[180:183], v[68:71]
	v_mfma_f32_16x16x32_bf16 v[64:67], v[196:199], v[180:183], v[64:67]
	s_setprio 0
	s_barrier
	ds_read_b128 v[152:155], v131 offset:16384
	ds_read_b128 v[156:159], v131 offset:18432
	ds_read_b128 v[160:163], v132 offset:16384
	ds_read_b128 v[164:167], v132 offset:18432
	ds_read_b128 v[168:171], v131 offset:20480
	ds_read_b128 v[172:175], v131 offset:22528
	ds_read_b128 v[176:179], v132 offset:20480
	ds_read_b128 v[180:183], v132 offset:22528
	s_lshl_b32 s8, s68, 7
	s_add_u32 s8, s54, s8
	s_addc_u32 s9, s55, 0
	s_mov_b32 s68, m0
	s_mov_b32 m0, s16
	s_nop 2
	global_load_lds_dwordx4 v128, s[8:9]
	s_mov_b32 m0, s68
	s_add_u32 s68, s8, 0x40000
	s_addc_u32 s69, s9, 0
	s_mov_b32 s72, m0
	s_mov_b32 m0, s20
	s_nop 2
	global_load_lds_dwordx4 v128, s[68:69]
	s_mov_b32 m0, s72
	s_barrier
	s_waitcnt lgkmcnt(0)
	s_setprio 1
	s_waitcnt lgkmcnt(7)
	v_mfma_f32_16x16x32_bf16 v[60:63], v[136:139], v[152:155], v[60:63]
	v_mfma_f32_16x16x32_bf16 v[56:59], v[140:143], v[152:155], v[56:59]
	s_waitcnt lgkmcnt(6)
	v_mfma_f32_16x16x32_bf16 v[52:55], v[136:139], v[156:159], v[52:55]
	v_mfma_f32_16x16x32_bf16 v[44:47], v[140:143], v[156:159], v[44:47]
	s_waitcnt lgkmcnt(3)
	v_mfma_f32_16x16x32_bf16 v[36:39], v[136:139], v[168:171], v[36:39]
	v_mfma_f32_16x16x32_bf16 v[28:31], v[140:143], v[168:171], v[28:31]
	s_waitcnt lgkmcnt(2)
	v_mfma_f32_16x16x32_bf16 v[20:23], v[136:139], v[172:175], v[20:23]
	v_mfma_f32_16x16x32_bf16 v[12:15], v[140:143], v[172:175], v[12:15]
	v_mfma_f32_16x16x32_bf16 v[60:63], v[144:147], v[160:163], v[60:63]
	v_mfma_f32_16x16x32_bf16 v[56:59], v[148:151], v[160:163], v[56:59]
	v_mfma_f32_16x16x32_bf16 v[52:55], v[144:147], v[164:167], v[52:55]
	v_mfma_f32_16x16x32_bf16 v[44:47], v[148:151], v[164:167], v[44:47]
	s_waitcnt lgkmcnt(1)
	v_mfma_f32_16x16x32_bf16 v[36:39], v[144:147], v[176:179], v[36:39]
	v_mfma_f32_16x16x32_bf16 v[28:31], v[148:151], v[176:179], v[28:31]
	s_waitcnt lgkmcnt(0)
	v_mfma_f32_16x16x32_bf16 v[20:23], v[144:147], v[180:183], v[20:23]
	v_mfma_f32_16x16x32_bf16 v[12:15], v[148:151], v[180:183], v[12:15]
	s_setprio 0
	s_barrier
; #define G_WAIT_V(n) asm volatile("s_waitcnt vmcnt(" #n ")" ::: "memory")
; #define G_WAIT_L(n) asm volatile("s_waitcnt lgkmcnt(" #n ")" ::: "memory")
; #define G_BAR do { asm volatile("" ::: "memory"); __builtin_amdgcn_s_barrier(); asm volatile("" ::: "memory"); } while (0)
; #define G_SCHED __builtin_amdgcn_sched_barrier(0)
; #define STG_A(b, h, kt) do { const unsigned char* _g = A + (size_t)KT_(kt) * ASTEP; \
;         dma16((const void*)(_g + (size_t)((h) * 128) * ROWB), ROWB ? aoff[0][0] : aoff[h][0], lds_u + SA_(b, h) + dma0); \
;         dma16((const void*)(_g + (size_t)((h) * 128 + 64) * ROWB), ROWB ? aoff[0][0] : aoff[h][1], lds_u + SA_(b, h) + dma1); } while (0)
; #define STG_B(b, h, kt) do { const unsigned char* _g = img + (size_t)KT_(kt) * 32768 + (h) * 16384; \
;         dma16((const void*)(_g + dma0), boffl, lds_u + SB_(b, h) + dma0); \
;         dma16((const void*)(_g + dma1), boffl, lds_u + SB_(b, h) + dma1); } while (0)
; #define LDA_(dst, b, h) do { _Pragma("unroll") for (int _m = 0; _m < 4; ++_m) { \
;         dst[_m].lo = *(LAS3 const i32x4d*)(ap0 + SA_(b, h) + _m * 2048); \
;         dst[_m].hi = *(LAS3 const i32x4d*)(ap1 + SA_(b, h) + _m * 2048); } } while (0)
; #define LDBF(dst, b, h) do { _Pragma("unroll") for (int _n = 0; _n < 2; ++_n) { \
;         dst[_n].lo = *(LAS3 const i32x4d*)(bp0 + (SB_(b, h) - 4 * GHTB) + _n * 8192); \
;         dst[_n].hi = *(LAS3 const i32x4d*)(bp1 + (SB_(b, h) - 4 * GHTB) + _n * 8192); } } while (0)
;     ...
;         STG_B(0, 1, t2);
;         G_WAIT_V(6); G_BAR; MMAD(1, 1, At, B1); G_BAR;
;         LDBF(B0, 1, 0); G_SCHED; LDA_(At, 1, 0); STG_A(0, 1, t2);
;         G_WAIT_L(8); G_BAR; G_WAIT_L(0); MMAD(0, 0, At, B0); G_BAR; G_SCHED;
;         LDBF(B1, 1, 1); STG_B(1, 0, t3);
;         G_BAR; G_WAIT_L(0); MMAD(0, 1, At, B1); G_BAR;
;         LDA_(At, 1, 1); STG_A(1, 0, t3);
;         G_BAR; G_WAIT_L(0); MMAD(1, 0, At, B0); G_BAR; G_SCHED;
	s_add_u32 s70, s70, 0x4000
	s_addc_u32 s71, s71, 0
	s_add_u32 s68, s70, s13
	s_addc_u32 s69, s71, s15
	s_mov_b32 s72, m0
	s_mov_b32 m0, s21
	s_nop 2
	global_load_lds_dwordx4 v135, s[68:69]
	s_mov_b32 m0, s72
	s_add_u32 s68, s70, s14
	s_addc_u32 s69, s71, s18
	s_mov_b32 s70, m0
	s_mov_b32 m0, s22
	s_nop 2
	global_load_lds_dwordx4 v135, s[68:69]
	s_mov_b32 m0, s70
	s_waitcnt vmcnt(10)
	s_barrier
	s_setprio 1
	v_mfma_f32_16x16x32_bf16 v[48:51], v[184:187], v[152:155], v[48:51]
	v_mfma_f32_16x16x32_bf16 v[40:43], v[188:191], v[152:155], v[40:43]
	v_mfma_f32_16x16x32_bf16 v[32:35], v[184:187], v[156:159], v[32:35]
	v_mfma_f32_16x16x32_bf16 v[24:27], v[188:191], v[156:159], v[24:27]
	v_mfma_f32_16x16x32_bf16 v[16:19], v[184:187], v[168:171], v[16:19]
	v_mfma_f32_16x16x32_bf16 v[8:11], v[188:191], v[168:171], v[8:11]
	v_mfma_f32_16x16x32_bf16 v[4:7], v[184:187], v[172:175], v[4:7]
	v_mfma_f32_16x16x32_bf16 v[0:3], v[188:191], v[172:175], v[0:3]
	v_mfma_f32_16x16x32_bf16 v[48:51], v[192:195], v[160:163], v[48:51]
	v_mfma_f32_16x16x32_bf16 v[40:43], v[196:199], v[160:163], v[40:43]
	v_mfma_f32_16x16x32_bf16 v[32:35], v[192:195], v[164:167], v[32:35]
	v_mfma_f32_16x16x32_bf16 v[24:27], v[196:199], v[164:167], v[24:27]
	v_mfma_f32_16x16x32_bf16 v[16:19], v[192:195], v[176:179], v[16:19]
	v_mfma_f32_16x16x32_bf16 v[8:11], v[196:199], v[176:179], v[8:11]
	v_mfma_f32_16x16x32_bf16 v[4:7], v[192:195], v[180:183], v[4:7]
	v_mfma_f32_16x16x32_bf16 v[0:3], v[196:199], v[180:183], v[0:3]
	s_setprio 0
	s_barrier
	ds_read_b128 v[136:139], v133 offset:32768
	ds_read_b128 v[140:143], v133 offset:40960
	ds_read_b128 v[144:147], v134 offset:32768
	ds_read_b128 v[148:151], v134 offset:40960
	ds_read_b128 v[152:155], v131 offset:32768
	ds_read_b128 v[156:159], v131 offset:34816
	ds_read_b128 v[160:163], v132 offset:32768
	ds_read_b128 v[164:167], v132 offset:34816
	ds_read_b128 v[168:171], v131 offset:36864
	ds_read_b128 v[172:175], v131 offset:38912
	ds_read_b128 v[176:179], v132 offset:36864
	ds_read_b128 v[180:183], v132 offset:38912
	s_add_u32 s68, s8, 0x80000
	s_addc_u32 s69, s9, 0
	s_mov_b32 s70, m0
	s_mov_b32 m0, s23
	s_nop 2
	global_load_lds_dwordx4 v128, s[68:69]
	s_mov_b32 m0, s70
	s_add_u32 s8, s8, 0xc0000
	s_addc_u32 s9, s9, 0
	s_mov_b32 s68, m0
	s_mov_b32 m0, s24
	s_nop 2
	global_load_lds_dwordx4 v128, s[8:9]
	s_mov_b32 m0, s68
	s_waitcnt lgkmcnt(8)
	s_waitcnt vmcnt(10)
	s_barrier
	s_waitcnt lgkmcnt(0)
	s_setprio 1
	s_waitcnt lgkmcnt(7)
	v_mfma_f32_16x16x32_bf16 v[124:127], v[136:139], v[152:155], v[124:127]
	v_mfma_f32_16x16x32_bf16 v[120:123], v[140:143], v[152:155], v[120:123]
	s_waitcnt lgkmcnt(6)
	v_mfma_f32_16x16x32_bf16 v[116:119], v[136:139], v[156:159], v[116:119]
	v_mfma_f32_16x16x32_bf16 v[108:111], v[140:143], v[156:159], v[108:111]
	s_waitcnt lgkmcnt(3)
	v_mfma_f32_16x16x32_bf16 v[100:103], v[136:139], v[168:171], v[100:103]
	v_mfma_f32_16x16x32_bf16 v[92:95], v[140:143], v[168:171], v[92:95]
	s_waitcnt lgkmcnt(2)
	v_mfma_f32_16x16x32_bf16 v[84:87], v[136:139], v[172:175], v[84:87]
	v_mfma_f32_16x16x32_bf16 v[76:79], v[140:143], v[172:175], v[76:79]
	v_mfma_f32_16x16x32_bf16 v[124:127], v[144:147], v[160:163], v[124:127]
	v_mfma_f32_16x16x32_bf16 v[120:123], v[148:151], v[160:163], v[120:123]
	v_mfma_f32_16x16x32_bf16 v[116:119], v[144:147], v[164:167], v[116:119]
	v_mfma_f32_16x16x32_bf16 v[108:111], v[148:151], v[164:167], v[108:111]
	s_waitcnt lgkmcnt(1)
	v_mfma_f32_16x16x32_bf16 v[100:103], v[144:147], v[176:179], v[100:103]
	v_mfma_f32_16x16x32_bf16 v[92:95], v[148:151], v[176:179], v[92:95]
	s_waitcnt lgkmcnt(0)
	v_mfma_f32_16x16x32_bf16 v[84:87], v[144:147], v[180:183], v[84:87]
	v_mfma_f32_16x16x32_bf16 v[76:79], v[148:151], v[180:183], v[76:79]
	s_setprio 0
	s_barrier
	s_min_u32 s8, s0, vcc_hi
	s_add_i32 s8, s8, vcc_lo
	s_and_b32 s68, s8, 31
	s_lshl_b32 s8, s68, 15
	s_add_u32 s69, s5, s8
	s_addc_u32 s70, s89, 0
	s_add_u32 s8, s69, s13
	ds_read_b128 v[184:187], v133 offset:49152
	ds_read_b128 v[188:191], v133 offset:57344
	ds_read_b128 v[192:195], v134 offset:49152
	ds_read_b128 v[196:199], v134 offset:57344
	s_addc_u32 s9, s70, s15
	s_mov_b32 s71, m0
	s_mov_b32 m0, s25
	s_nop 2
	global_load_lds_dwordx4 v135, s[8:9]
	s_mov_b32 m0, s71
	s_add_u32 s8, s69, s14
	s_addc_u32 s9, s70, s18
	s_mov_b32 s71, m0
	s_mov_b32 m0, s26
	s_nop 2
	global_load_lds_dwordx4 v135, s[8:9]
	s_mov_b32 m0, s71
	s_waitcnt vmcnt(10)
	s_barrier
; #define G_WAIT_V(n) asm volatile("s_waitcnt vmcnt(" #n ")" ::: "memory")
; #define G_WAIT_L(n) asm volatile("s_waitcnt lgkmcnt(" #n ")" ::: "memory")
; #define G_BAR do { asm volatile("" ::: "memory"); __builtin_amdgcn_s_barrier(); asm volatile("" ::: "memory"); } while (0)
; #define G_SCHED __builtin_amdgcn_sched_barrier(0)
; #define STG_A(b, h, kt) do { const unsigned char* _g = A + (size_t)KT_(kt) * ASTEP; \
;         dma16((const void*)(_g + (size_t)((h) * 128) * ROWB), ROWB ? aoff[0][0] : aoff[h][0], lds_u + SA_(b, h) + dma0); \
;         dma16((const void*)(_g + (size_t)((h) * 128 + 64) * ROWB), ROWB ? aoff[0][0] : aoff[h][1], lds_u + SA_(b, h) + dma1); } while (0)
; #define STG_B(b, h, kt) do { const unsigned char* _g = img + (size_t)KT_(kt) * 32768 + (h) * 16384; \
;         dma16((const void*)(_g + dma0), boffl, lds_u + SB_(b, h) + dma0); \
;         dma16((const void*)(_g + dma1), boffl, lds_u + SB_(b, h) + dma1); } while (0)
; #define LDA_(dst, b, h) do { _Pragma("unroll") for (int _m = 0; _m < 4; ++_m) { \
;         dst[_m].lo = *(LAS3 const i32x4d*)(ap0 + SA_(b, h) + _m * 2048); \
;         dst[_m].hi = *(LAS3 const i32x4d*)(ap1 + SA_(b, h) + _m * 2048); } } while (0)
;     ...
;         LDA_(At, 1, 1); STG_A(1, 0, t3);
;         G_BAR; G_WAIT_L(0); MMAD(1, 0, At, B0); G_BAR; G_SCHED;
;         STG_B(1, 1, t3);
;         G_WAIT_V(6); G_BAR; MMAD(1, 1, At, B1); G_BAR;
;     }
	s_waitcnt lgkmcnt(0)
	s_setprio 1
	s_waitcnt lgkmcnt(3)
	v_mfma_f32_16x16x32_bf16 v[112:115], v[184:187], v[152:155], v[112:115]
	s_waitcnt lgkmcnt(2)
	v_mfma_f32_16x16x32_bf16 v[104:107], v[188:191], v[152:155], v[104:107]
	v_mfma_f32_16x16x32_bf16 v[96:99], v[184:187], v[156:159], v[96:99]
	v_mfma_f32_16x16x32_bf16 v[88:91], v[188:191], v[156:159], v[88:91]
	v_mfma_f32_16x16x32_bf16 v[80:83], v[184:187], v[168:171], v[80:83]
	v_mfma_f32_16x16x32_bf16 v[72:75], v[188:191], v[168:171], v[72:75]
	v_mfma_f32_16x16x32_bf16 v[68:71], v[184:187], v[172:175], v[68:71]
	v_mfma_f32_16x16x32_bf16 v[64:67], v[188:191], v[172:175], v[64:67]
	s_waitcnt lgkmcnt(1)
	v_mfma_f32_16x16x32_bf16 v[112:115], v[192:195], v[160:163], v[112:115]
	s_waitcnt lgkmcnt(0)
	v_mfma_f32_16x16x32_bf16 v[104:107], v[196:199], v[160:163], v[104:107]
	v_mfma_f32_16x16x32_bf16 v[96:99], v[192:195], v[164:167], v[96:99]
	v_mfma_f32_16x16x32_bf16 v[88:91], v[196:199], v[164:167], v[88:91]
	v_mfma_f32_16x16x32_bf16 v[80:83], v[192:195], v[176:179], v[80:83]
	v_mfma_f32_16x16x32_bf16 v[72:75], v[196:199], v[176:179], v[72:75]
	v_mfma_f32_16x16x32_bf16 v[68:71], v[192:195], v[180:183], v[68:71]
	v_mfma_f32_16x16x32_bf16 v[64:67], v[196:199], v[180:183], v[64:67]
	s_setprio 0
	s_barrier
	ds_read_b128 v[152:155], v131 offset:49152
	ds_read_b128 v[156:159], v131 offset:51200
	ds_read_b128 v[160:163], v132 offset:49152
	ds_read_b128 v[164:167], v132 offset:51200
	ds_read_b128 v[168:171], v131 offset:53248
	ds_read_b128 v[172:175], v131 offset:55296
	ds_read_b128 v[176:179], v132 offset:53248
	ds_read_b128 v[180:183], v132 offset:55296
	s_lshl_b32 s8, s68, 7
	s_add_u32 s8, s54, s8
	s_addc_u32 s9, s55, 0
	s_mov_b32 s68, m0
	s_mov_b32 m0, s27
	s_nop 2
	global_load_lds_dwordx4 v128, s[8:9]
	s_mov_b32 m0, s68
	s_add_u32 s8, s8, 0x40000
	s_addc_u32 s9, s9, 0
	s_mov_b32 s68, m0
	s_mov_b32 m0, s28
	s_nop 2
	global_load_lds_dwordx4 v128, s[8:9]
	s_mov_b32 m0, s68
	s_barrier
	s_waitcnt lgkmcnt(0)
	s_setprio 1
	s_waitcnt lgkmcnt(7)
	v_mfma_f32_16x16x32_bf16 v[60:63], v[136:139], v[152:155], v[60:63]
	v_mfma_f32_16x16x32_bf16 v[56:59], v[140:143], v[152:155], v[56:59]
	s_waitcnt lgkmcnt(6)
	v_mfma_f32_16x16x32_bf16 v[52:55], v[136:139], v[156:159], v[52:55]
	v_mfma_f32_16x16x32_bf16 v[44:47], v[140:143], v[156:159], v[44:47]
	s_waitcnt lgkmcnt(3)
	v_mfma_f32_16x16x32_bf16 v[36:39], v[136:139], v[168:171], v[36:39]
	v_mfma_f32_16x16x32_bf16 v[28:31], v[140:143], v[168:171], v[28:31]
	s_waitcnt lgkmcnt(2)
	v_mfma_f32_16x16x32_bf16 v[20:23], v[136:139], v[172:175], v[20:23]
	v_mfma_f32_16x16x32_bf16 v[12:15], v[140:143], v[172:175], v[12:15]
	v_mfma_f32_16x16x32_bf16 v[60:63], v[144:147], v[160:163], v[60:63]
	v_mfma_f32_16x16x32_bf16 v[56:59], v[148:151], v[160:163], v[56:59]
	v_mfma_f32_16x16x32_bf16 v[52:55], v[144:147], v[164:167], v[52:55]
	v_mfma_f32_16x16x32_bf16 v[44:47], v[148:151], v[164:167], v[44:47]
	s_waitcnt lgkmcnt(1)
	v_mfma_f32_16x16x32_bf16 v[36:39], v[144:147], v[176:179], v[36:39]
	v_mfma_f32_16x16x32_bf16 v[28:31], v[148:151], v[176:179], v[28:31]
	s_waitcnt lgkmcnt(0)
	v_mfma_f32_16x16x32_bf16 v[20:23], v[144:147], v[180:183], v[20:23]
	v_mfma_f32_16x16x32_bf16 v[12:15], v[148:151], v[180:183], v[12:15]
	s_setprio 0
	s_barrier
	s_add_u32 s68, s69, 0x4000
	s_addc_u32 s69, s70, 0
	s_add_u32 s8, s68, s13
	s_addc_u32 s9, s69, s15
	s_mov_b32 s70, m0
	s_mov_b32 m0, s29
	s_nop 2
	global_load_lds_dwordx4 v135, s[8:9]
	s_mov_b32 m0, s70
	s_add_u32 s8, s68, s14
	s_addc_u32 s9, s69, s18
	s_mov_b32 s68, m0
	s_mov_b32 m0, s30
	s_nop 2
	global_load_lds_dwordx4 v135, s[8:9]
	s_mov_b32 m0, s68
	s_waitcnt vmcnt(10)
	s_barrier
	s_setprio 1
	v_mfma_f32_16x16x32_bf16 v[48:51], v[184:187], v[152:155], v[48:51]
	v_mfma_f32_16x16x32_bf16 v[40:43], v[188:191], v[152:155], v[40:43]
	v_mfma_f32_16x16x32_bf16 v[32:35], v[184:187], v[156:159], v[32:35]
	v_mfma_f32_16x16x32_bf16 v[24:27], v[188:191], v[156:159], v[24:27]
	v_mfma_f32_16x16x32_bf16 v[16:19], v[184:187], v[168:171], v[16:19]
	v_mfma_f32_16x16x32_bf16 v[8:11], v[188:191], v[168:171], v[8:11]
	v_mfma_f32_16x16x32_bf16 v[4:7], v[184:187], v[172:175], v[4:7]
	v_mfma_f32_16x16x32_bf16 v[0:3], v[188:191], v[172:175], v[0:3]
	v_mfma_f32_16x16x32_bf16 v[48:51], v[192:195], v[160:163], v[48:51]
	v_mfma_f32_16x16x32_bf16 v[40:43], v[196:199], v[160:163], v[40:43]
	v_mfma_f32_16x16x32_bf16 v[32:35], v[192:195], v[164:167], v[32:35]
	v_mfma_f32_16x16x32_bf16 v[24:27], v[196:199], v[164:167], v[24:27]
	v_mfma_f32_16x16x32_bf16 v[16:19], v[192:195], v[176:179], v[16:19]
	v_mfma_f32_16x16x32_bf16 v[8:11], v[196:199], v[176:179], v[8:11]
	v_mfma_f32_16x16x32_bf16 v[4:7], v[192:195], v[180:183], v[4:7]
	v_mfma_f32_16x16x32_bf16 v[0:3], v[196:199], v[180:183], v[0:3]
	s_setprio 0
	s_barrier
	s_add_i32 s0, s0, 2
	s_cmp_ge_u32 s1, s34
	s_cbranch_scc0 .LBB0_90
	s_waitcnt vmcnt(0)
	s_waitcnt lgkmcnt(0)
	s_mov_b32 s0, s10
	s_cmp_eq_u32 s0, 0
	s_cbranch_scc0 .LBB0_93
	s_barrier

; #define G_WAIT_V(n) asm volatile("s_waitcnt vmcnt(" #n ")" ::: "memory")
; #define G_WAIT_L(n) asm volatile("s_waitcnt lgkmcnt(" #n ")" ::: "memory")
; #define G_BAR do { asm volatile("" ::: "memory"); __builtin_amdgcn_s_barrier(); asm volatile("" ::: "memory"); } while (0)
; #define G_SCHED __builtin_amdgcn_sched_barrier(0)
; #define STG_A(b, h, kt) do { const unsigned char* _g = A + (size_t)KT_(kt) * ASTEP; \
;         dma16((const void*)(_g + (size_t)((h) * 128) * ROWB), ROWB ? aoff[0][0] : aoff[h][0], lds_u + SA_(b, h) + dma0); \
;         dma16((const void*)(_g + (size_t)((h) * 128 + 64) * ROWB), ROWB ? aoff[0][0] : aoff[h][1], lds_u + SA_(b, h) + dma1); } while (0)
; #define STG_B(b, h, kt) do { const unsigned char* _g = img + (size_t)KT_(kt) * 32768 + (h) * 16384; \
;         dma16((const void*)(_g + dma0), boffl, lds_u + SB_(b, h) + dma0); \
;         dma16((const void*)(_g + dma1), boffl, lds_u + SB_(b, h) + dma1); } while (0)
; #define LDA_(dst, b, h) do { _Pragma("unroll") for (int _m = 0; _m < 4; ++_m) { \
;         dst[_m].lo = *(LAS3 const i32x4d*)(ap0 + SA_(b, h) + _m * 2048); \
;         dst[_m].hi = *(LAS3 const i32x4d*)(ap1 + SA_(b, h) + _m * 2048); } } while (0)
; #define LDBF(dst, b, h) do { _Pragma("unroll") for (int _n = 0; _n < 2; ++_n) { \
;         dst[_n].lo = *(LAS3 const i32x4d*)(bp0 + (SB_(b, h) - 4 * GHTB) + _n * 8192); \
;         dst[_n].hi = *(LAS3 const i32x4d*)(bp1 + (SB_(b, h) - 4 * GHTB) + _n * 8192); } } while (0)
;     ...
;     for (int t = 0; t < nt; t += 2) {
;         const int t1 = (t + 1 < nt) ? t + 1 : nt - 1, t2 = (t + 2 < nt) ? t + 2 : nt - 1, t3 = (t + 3 < nt) ? t + 3 : nt - 1;
;         LDBF(B0, 0, 0); G_SCHED; LDA_(At, 0, 0); STG_A(1, 1, t1);
;         G_WAIT_L(8); G_BAR; G_WAIT_L(0); MMAD(0, 0, At, B0); G_BAR; G_SCHED;
;         LDBF(B1, 0, 1); STG_B(0, 0, t2);
;         G_BAR; G_WAIT_L(0); MMAD(0, 1, At, B1); G_BAR;
;         LDA_(At, 0, 1); STG_A(0, 0, t2);
;         G_BAR; G_WAIT_L(0); MMAD(1, 0, At, B0); G_BAR; G_SCHED;
;         STG_B(0, 1, t2);
;         G_WAIT_V(6); G_BAR; MMAD(1, 1, At, B1); G_BAR;
.LBB0_278:
	ds_read_b128 v[136:139], v132
	ds_read_b128 v[140:143], v132 offset:8192
	ds_read_b128 v[144:147], v133
	ds_read_b128 v[148:151], v133 offset:8192
	s_add_i32 s90, s26, 2
	s_add_i32 s26, s26, 4
	s_min_u32 s68, s26, 31
	ds_read_b128 v[152:155], v129
	ds_read_b128 v[156:159], v129 offset:2048
	ds_read_b128 v[160:163], v131
	ds_read_b128 v[164:167], v131 offset:2048
	ds_read_b128 v[168:171], v129 offset:4096
	ds_read_b128 v[172:175], v129 offset:6144
	ds_read_b128 v[176:179], v131 offset:4096
	ds_read_b128 v[180:183], v131 offset:6144
	s_add_u32 s26, s16, 0x80080
	s_addc_u32 s27, s17, 0
	s_mov_b32 s69, m0
	s_mov_b32 m0, s71
	s_nop 2
	global_load_lds_dwordx4 v128, s[26:27]
	s_mov_b32 m0, s69
	s_add_u32 s26, s16, 0xc0080
	s_addc_u32 s27, s17, 0
	s_mov_b32 s69, m0
	s_mov_b32 m0, s86
	s_nop 2
	global_load_lds_dwordx4 v128, s[26:27]
	s_mov_b32 m0, s69
	s_waitcnt lgkmcnt(8)
	s_waitcnt vmcnt(10)
	s_barrier
	s_waitcnt lgkmcnt(0)
	s_setprio 1
	s_waitcnt lgkmcnt(7)
	v_mfma_f32_16x16x32_bf16 v[124:127], v[136:139], v[152:155], v[124:127]
	v_mfma_f32_16x16x32_bf16 v[120:123], v[140:143], v[152:155], v[120:123]
	s_waitcnt lgkmcnt(6)
	v_mfma_f32_16x16x32_bf16 v[112:115], v[136:139], v[156:159], v[112:115]
	v_mfma_f32_16x16x32_bf16 v[108:111], v[140:143], v[156:159], v[108:111]
	s_waitcnt lgkmcnt(3)
	v_mfma_f32_16x16x32_bf16 v[96:99], v[136:139], v[168:171], v[96:99]
	v_mfma_f32_16x16x32_bf16 v[92:95], v[140:143], v[168:171], v[92:95]
	s_waitcnt lgkmcnt(2)
	v_mfma_f32_16x16x32_bf16 v[80:83], v[136:139], v[172:175], v[80:83]
	v_mfma_f32_16x16x32_bf16 v[76:79], v[140:143], v[172:175], v[76:79]
	v_mfma_f32_16x16x32_bf16 v[124:127], v[144:147], v[160:163], v[124:127]
	v_mfma_f32_16x16x32_bf16 v[120:123], v[148:151], v[160:163], v[120:123]
	v_mfma_f32_16x16x32_bf16 v[112:115], v[144:147], v[164:167], v[112:115]
	v_mfma_f32_16x16x32_bf16 v[108:111], v[148:151], v[164:167], v[108:111]
	s_waitcnt lgkmcnt(1)
	v_mfma_f32_16x16x32_bf16 v[96:99], v[144:147], v[176:179], v[96:99]
	v_mfma_f32_16x16x32_bf16 v[92:95], v[148:151], v[176:179], v[92:95]
	s_waitcnt lgkmcnt(0)
	v_mfma_f32_16x16x32_bf16 v[80:83], v[144:147], v[180:183], v[80:83]
	v_mfma_f32_16x16x32_bf16 v[76:79], v[148:151], v[180:183], v[76:79]
	s_setprio 0
	s_barrier
	s_lshl_b32 s26, s68, 15
	s_add_u32 s72, s88, s26
	s_addc_u32 s73, s89, 0
	s_add_u32 s26, s72, s20
	ds_read_b128 v[184:187], v132 offset:16384
	ds_read_b128 v[188:191], v132 offset:24576
	ds_read_b128 v[192:195], v133 offset:16384
	ds_read_b128 v[196:199], v133 offset:24576
	s_addc_u32 s27, s73, s22
	s_mov_b32 s69, m0
	s_mov_b32 m0, s25
	s_nop 2
	global_load_lds_dwordx4 v134, s[26:27]
	s_mov_b32 m0, s69
	s_add_u32 s26, s72, s21
	s_addc_u32 s27, s73, s28
	s_mov_b32 s69, m0
	s_mov_b32 m0, s29
	s_nop 2
	global_load_lds_dwordx4 v134, s[26:27]
	s_mov_b32 m0, s69
	s_waitcnt vmcnt(10)
	s_barrier
	s_waitcnt lgkmcnt(0)
	s_setprio 1
	s_waitcnt lgkmcnt(3)
	v_mfma_f32_16x16x32_bf16 v[116:119], v[184:187], v[152:155], v[116:119]
	s_waitcnt lgkmcnt(2)
	v_mfma_f32_16x16x32_bf16 v[104:107], v[188:191], v[152:155], v[104:107]
	v_mfma_f32_16x16x32_bf16 v[100:103], v[184:187], v[156:159], v[100:103]
	v_mfma_f32_16x16x32_bf16 v[88:91], v[188:191], v[156:159], v[88:91]
	v_mfma_f32_16x16x32_bf16 v[84:87], v[184:187], v[168:171], v[84:87]
	v_mfma_f32_16x16x32_bf16 v[72:75], v[188:191], v[168:171], v[72:75]
	v_mfma_f32_16x16x32_bf16 v[68:71], v[184:187], v[172:175], v[68:71]
	v_mfma_f32_16x16x32_bf16 v[64:67], v[188:191], v[172:175], v[64:67]
	s_waitcnt lgkmcnt(1)
	v_mfma_f32_16x16x32_bf16 v[116:119], v[192:195], v[160:163], v[116:119]
	s_waitcnt lgkmcnt(0)
	v_mfma_f32_16x16x32_bf16 v[104:107], v[196:199], v[160:163], v[104:107]
	v_mfma_f32_16x16x32_bf16 v[100:103], v[192:195], v[164:167], v[100:103]
	v_mfma_f32_16x16x32_bf16 v[88:91], v[196:199], v[164:167], v[88:91]
	v_mfma_f32_16x16x32_bf16 v[84:87], v[192:195], v[176:179], v[84:87]
	v_mfma_f32_16x16x32_bf16 v[72:75], v[196:199], v[176:179], v[72:75]
	v_mfma_f32_16x16x32_bf16 v[68:71], v[192:195], v[180:183], v[68:71]
	v_mfma_f32_16x16x32_bf16 v[64:67], v[196:199], v[180:183], v[64:67]
	s_setprio 0
	s_barrier
	ds_read_b128 v[152:155], v129 offset:16384
	ds_read_b128 v[156:159], v129 offset:18432
	ds_read_b128 v[160:163], v131 offset:16384
	ds_read_b128 v[164:167], v131 offset:18432
	ds_read_b128 v[168:171], v129 offset:20480
	ds_read_b128 v[172:175], v129 offset:22528
	ds_read_b128 v[176:179], v131 offset:20480
	ds_read_b128 v[180:183], v131 offset:22528
	s_lshl_b32 s26, s68, 7
	s_add_u32 s26, s60, s26
	s_addc_u32 s27, s61, 0
	s_mov_b32 s68, m0
	s_mov_b32 m0, s23
	s_nop 2
	global_load_lds_dwordx4 v128, s[26:27]
	s_mov_b32 m0, s68
	s_add_u32 s68, s26, 0x40000
	s_addc_u32 s69, s27, 0
	s_mov_b32 s74, m0
	s_mov_b32 m0, s30
	s_nop 2
	global_load_lds_dwordx4 v128, s[68:69]
	s_mov_b32 m0, s74
	s_barrier
	s_waitcnt lgkmcnt(0)
	s_setprio 1
	s_waitcnt lgkmcnt(7)
	v_mfma_f32_16x16x32_bf16 v[60:63], v[136:139], v[152:155], v[60:63]
	v_mfma_f32_16x16x32_bf16 v[56:59], v[140:143], v[152:155], v[56:59]
	s_waitcnt lgkmcnt(6)
	v_mfma_f32_16x16x32_bf16 v[48:51], v[136:139], v[156:159], v[48:51]
	v_mfma_f32_16x16x32_bf16 v[44:47], v[140:143], v[156:159], v[44:47]
	s_waitcnt lgkmcnt(3)
	v_mfma_f32_16x16x32_bf16 v[32:35], v[136:139], v[168:171], v[32:35]
	v_mfma_f32_16x16x32_bf16 v[28:31], v[140:143], v[168:171], v[28:31]
	s_waitcnt lgkmcnt(2)
	v_mfma_f32_16x16x32_bf16 v[16:19], v[136:139], v[172:175], v[16:19]
	v_mfma_f32_16x16x32_bf16 v[12:15], v[140:143], v[172:175], v[12:15]
	v_mfma_f32_16x16x32_bf16 v[60:63], v[144:147], v[160:163], v[60:63]
	v_mfma_f32_16x16x32_bf16 v[56:59], v[148:151], v[160:163], v[56:59]
	v_mfma_f32_16x16x32_bf16 v[48:51], v[144:147], v[164:167], v[48:51]
	v_mfma_f32_16x16x32_bf16 v[44:47], v[148:151], v[164:167], v[44:47]
	s_waitcnt lgkmcnt(1)
	v_mfma_f32_16x16x32_bf16 v[32:35], v[144:147], v[176:179], v[32:35]
	v_mfma_f32_16x16x32_bf16 v[28:31], v[148:151], v[176:179], v[28:31]
	s_waitcnt lgkmcnt(0)
	v_mfma_f32_16x16x32_bf16 v[16:19], v[144:147], v[180:183], v[16:19]
	v_mfma_f32_16x16x32_bf16 v[12:15], v[148:151], v[180:183], v[12:15]
	s_setprio 0
	s_barrier
; #define G_WAIT_V(n) asm volatile("s_waitcnt vmcnt(" #n ")" ::: "memory")
; #define G_WAIT_L(n) asm volatile("s_waitcnt lgkmcnt(" #n ")" ::: "memory")
; #define G_BAR do { asm volatile("" ::: "memory"); __builtin_amdgcn_s_barrier(); asm volatile("" ::: "memory"); } while (0)
; #define G_SCHED __builtin_amdgcn_sched_barrier(0)
; #define STG_A(b, h, kt) do { const unsigned char* _g = A + (size_t)KT_(kt) * ASTEP; \
;         dma16((const void*)(_g + (size_t)((h) * 128) * ROWB), ROWB ? aoff[0][0] : aoff[h][0], lds_u + SA_(b, h) + dma0); \
;         dma16((const void*)(_g + (size_t)((h) * 128 + 64) * ROWB), ROWB ? aoff[0][0] : aoff[h][1], lds_u + SA_(b, h) + dma1); } while (0)
; #define STG_B(b, h, kt) do { const unsigned char* _g = img + (size_t)KT_(kt) * 32768 + (h) * 16384; \
;         dma16((const void*)(_g + dma0), boffl, lds_u + SB_(b, h) + dma0); \
;         dma16((const void*)(_g + dma1), boffl, lds_u + SB_(b, h) + dma1); } while (0)
; #define LDA_(dst, b, h) do { _Pragma("unroll") for (int _m = 0; _m < 4; ++_m) { \
;         dst[_m].lo = *(LAS3 const i32x4d*)(ap0 + SA_(b, h) + _m * 2048); \
;         dst[_m].hi = *(LAS3 const i32x4d*)(ap1 + SA_(b, h) + _m * 2048); } } while (0)
; #define LDBF(dst, b, h) do { _Pragma("unroll") for (int _n = 0; _n < 2; ++_n) { \
;         dst[_n].lo = *(LAS3 const i32x4d*)(bp0 + (SB_(b, h) - 4 * GHTB) + _n * 8192); \
;         dst[_n].hi = *(LAS3 const i32x4d*)(bp1 + (SB_(b, h) - 4 * GHTB) + _n * 8192); } } while (0)
;     ...
;         STG_B(0, 1, t2);
;         G_WAIT_V(6); G_BAR; MMAD(1, 1, At, B1); G_BAR;
;         LDBF(B0, 1, 0); G_SCHED; LDA_(At, 1, 0); STG_A(0, 1, t2);
;         G_WAIT_L(8); G_BAR; G_WAIT_L(0); MMAD(0, 0, At, B0); G_BAR; G_SCHED;
;         LDBF(B1, 1, 1); STG_B(1, 0, t3);
;         G_BAR; G_WAIT_L(0); MMAD(0, 1, At, B1); G_BAR;
;         LDA_(At, 1, 1); STG_A(1, 0, t3);
;         G_BAR; G_WAIT_L(0); MMAD(1, 0, At, B0); G_BAR; G_SCHED;
	s_add_u32 s72, s72, 0x4000
	s_addc_u32 s73, s73, 0
	s_add_u32 s68, s72, s20
	s_addc_u32 s69, s73, s22
	s_mov_b32 s74, m0
	s_mov_b32 m0, s31
	s_nop 2
	global_load_lds_dwordx4 v134, s[68:69]
	s_mov_b32 m0, s74
	s_add_u32 s68, s72, s21
	s_addc_u32 s69, s73, s28
	s_mov_b32 s72, m0
	s_mov_b32 m0, s33
	s_nop 2
	global_load_lds_dwordx4 v134, s[68:69]
	s_mov_b32 m0, s72
	s_waitcnt vmcnt(10)
	s_barrier
	s_setprio 1
	v_mfma_f32_16x16x32_bf16 v[52:55], v[184:187], v[152:155], v[52:55]
	v_mfma_f32_16x16x32_bf16 v[40:43], v[188:191], v[152:155], v[40:43]
	v_mfma_f32_16x16x32_bf16 v[36:39], v[184:187], v[156:159], v[36:39]
	v_mfma_f32_16x16x32_bf16 v[24:27], v[188:191], v[156:159], v[24:27]
	v_mfma_f32_16x16x32_bf16 v[20:23], v[184:187], v[168:171], v[20:23]
	v_mfma_f32_16x16x32_bf16 v[8:11], v[188:191], v[168:171], v[8:11]
	v_mfma_f32_16x16x32_bf16 v[4:7], v[184:187], v[172:175], v[4:7]
	v_mfma_f32_16x16x32_bf16 v[0:3], v[188:191], v[172:175], v[0:3]
	v_mfma_f32_16x16x32_bf16 v[52:55], v[192:195], v[160:163], v[52:55]
	v_mfma_f32_16x16x32_bf16 v[40:43], v[196:199], v[160:163], v[40:43]
	v_mfma_f32_16x16x32_bf16 v[36:39], v[192:195], v[164:167], v[36:39]
	v_mfma_f32_16x16x32_bf16 v[24:27], v[196:199], v[164:167], v[24:27]
	v_mfma_f32_16x16x32_bf16 v[20:23], v[192:195], v[176:179], v[20:23]
	v_mfma_f32_16x16x32_bf16 v[8:11], v[196:199], v[176:179], v[8:11]
	v_mfma_f32_16x16x32_bf16 v[4:7], v[192:195], v[180:183], v[4:7]
	v_mfma_f32_16x16x32_bf16 v[0:3], v[196:199], v[180:183], v[0:3]
	s_setprio 0
	s_barrier
	ds_read_b128 v[136:139], v132 offset:32768
	ds_read_b128 v[140:143], v132 offset:40960
	ds_read_b128 v[144:147], v133 offset:32768
	ds_read_b128 v[148:151], v133 offset:40960
	ds_read_b128 v[152:155], v129 offset:32768
	ds_read_b128 v[156:159], v129 offset:34816
	ds_read_b128 v[160:163], v131 offset:32768
	ds_read_b128 v[164:167], v131 offset:34816
	ds_read_b128 v[168:171], v129 offset:36864
	ds_read_b128 v[172:175], v129 offset:38912
	ds_read_b128 v[176:179], v131 offset:36864
	ds_read_b128 v[180:183], v131 offset:38912
	s_add_u32 s68, s26, 0x80000
	s_addc_u32 s69, s27, 0
	s_mov_b32 s72, m0
	s_mov_b32 m0, s34
	s_nop 2
	global_load_lds_dwordx4 v128, s[68:69]
	s_mov_b32 m0, s72
	s_add_u32 s26, s26, 0xc0000
	s_addc_u32 s27, s27, 0
	s_mov_b32 s68, m0
	s_mov_b32 m0, s54
	s_nop 2
	global_load_lds_dwordx4 v128, s[26:27]
	s_mov_b32 m0, s68
	s_waitcnt lgkmcnt(8)
	s_waitcnt vmcnt(10)
	s_barrier
	s_waitcnt lgkmcnt(0)
	s_setprio 1
	s_waitcnt lgkmcnt(7)
	v_mfma_f32_16x16x32_bf16 v[124:127], v[136:139], v[152:155], v[124:127]
	v_mfma_f32_16x16x32_bf16 v[120:123], v[140:143], v[152:155], v[120:123]
	s_waitcnt lgkmcnt(6)
	v_mfma_f32_16x16x32_bf16 v[112:115], v[136:139], v[156:159], v[112:115]
	v_mfma_f32_16x16x32_bf16 v[108:111], v[140:143], v[156:159], v[108:111]
	s_waitcnt lgkmcnt(3)
	v_mfma_f32_16x16x32_bf16 v[96:99], v[136:139], v[168:171], v[96:99]
	v_mfma_f32_16x16x32_bf16 v[92:95], v[140:143], v[168:171], v[92:95]
	s_waitcnt lgkmcnt(2)
	v_mfma_f32_16x16x32_bf16 v[80:83], v[136:139], v[172:175], v[80:83]
	v_mfma_f32_16x16x32_bf16 v[76:79], v[140:143], v[172:175], v[76:79]
	v_mfma_f32_16x16x32_bf16 v[124:127], v[144:147], v[160:163], v[124:127]
	v_mfma_f32_16x16x32_bf16 v[120:123], v[148:151], v[160:163], v[120:123]
	v_mfma_f32_16x16x32_bf16 v[112:115], v[144:147], v[164:167], v[112:115]
	v_mfma_f32_16x16x32_bf16 v[108:111], v[148:151], v[164:167], v[108:111]
	s_waitcnt lgkmcnt(1)
	v_mfma_f32_16x16x32_bf16 v[96:99], v[144:147], v[176:179], v[96:99]
	v_mfma_f32_16x16x32_bf16 v[92:95], v[148:151], v[176:179], v[92:95]
	s_waitcnt lgkmcnt(0)
	v_mfma_f32_16x16x32_bf16 v[80:83], v[144:147], v[180:183], v[80:83]
	v_mfma_f32_16x16x32_bf16 v[76:79], v[148:151], v[180:183], v[76:79]
	s_setprio 0
	s_barrier
	s_min_u32 s26, s90, 28
	s_add_i32 s68, s26, 3
	s_lshl_b32 s26, s68, 15
	s_add_u32 s69, s88, s26
	s_addc_u32 s72, s89, 0
	s_add_u32 s26, s69, s20
	ds_read_b128 v[184:187], v132 offset:49152
	ds_read_b128 v[188:191], v132 offset:57344
	ds_read_b128 v[192:195], v133 offset:49152
	ds_read_b128 v[196:199], v133 offset:57344
	s_addc_u32 s27, s72, s22
	s_mov_b32 s73, m0
	s_mov_b32 m0, s55
	s_nop 2
	global_load_lds_dwordx4 v134, s[26:27]
	s_mov_b32 m0, s73
	s_add_u32 s26, s69, s21
	s_addc_u32 s27, s72, s28
	s_mov_b32 s73, m0
	s_mov_b32 m0, s56
	s_nop 2
	global_load_lds_dwordx4 v134, s[26:27]
	s_mov_b32 m0, s73
	s_waitcnt vmcnt(10)
	s_barrier
; #define G_WAIT_V(n) asm volatile("s_waitcnt vmcnt(" #n ")" ::: "memory")
; #define G_WAIT_L(n) asm volatile("s_waitcnt lgkmcnt(" #n ")" ::: "memory")
; #define G_BAR do { asm volatile("" ::: "memory"); __builtin_amdgcn_s_barrier(); asm volatile("" ::: "memory"); } while (0)
; #define G_SCHED __builtin_amdgcn_sched_barrier(0)
; #define STG_A(b, h, kt) do { const unsigned char* _g = A + (size_t)KT_(kt) * ASTEP; \
;         dma16((const void*)(_g + (size_t)((h) * 128) * ROWB), ROWB ? aoff[0][0] : aoff[h][0], lds_u + SA_(b, h) + dma0); \
;         dma16((const void*)(_g + (size_t)((h) * 128 + 64) * ROWB), ROWB ? aoff[0][0] : aoff[h][1], lds_u + SA_(b, h) + dma1); } while (0)
; #define STG_B(b, h, kt) do { const unsigned char* _g = img + (size_t)KT_(kt) * 32768 + (h) * 16384; \
;         dma16((const void*)(_g + dma0), boffl, lds_u + SB_(b, h) + dma0); \
;         dma16((const void*)(_g + dma1), boffl, lds_u + SB_(b, h) + dma1); } while (0)
; #define LDA_(dst, b, h) do { _Pragma("unroll") for (int _m = 0; _m < 4; ++_m) { \
;         dst[_m].lo = *(LAS3 const i32x4d*)(ap0 + SA_(b, h) + _m * 2048); \
;         dst[_m].hi = *(LAS3 const i32x4d*)(ap1 + SA_(b, h) + _m * 2048); } } while (0)
;     ...
;         LDA_(At, 1, 1); STG_A(1, 0, t3);
;         G_BAR; G_WAIT_L(0); MMAD(1, 0, At, B0); G_BAR; G_SCHED;
;         STG_B(1, 1, t3);
;         G_WAIT_V(6); G_BAR; MMAD(1, 1, At, B1); G_BAR;
;     }
;     G_WAIT_V(0); G_WAIT_L(0);
;     { int wr0 = wid >> 2; asm volatile("" : "+s"(wr0)); if (wr0 == 0) G_BAR; }
;     G_BAR;
	s_waitcnt lgkmcnt(0)
	s_setprio 1
	s_waitcnt lgkmcnt(3)
	v_mfma_f32_16x16x32_bf16 v[116:119], v[184:187], v[152:155], v[116:119]
	s_waitcnt lgkmcnt(2)
	v_mfma_f32_16x16x32_bf16 v[104:107], v[188:191], v[152:155], v[104:107]
	v_mfma_f32_16x16x32_bf16 v[100:103], v[184:187], v[156:159], v[100:103]
	v_mfma_f32_16x16x32_bf16 v[88:91], v[188:191], v[156:159], v[88:91]
	v_mfma_f32_16x16x32_bf16 v[84:87], v[184:187], v[168:171], v[84:87]
	v_mfma_f32_16x16x32_bf16 v[72:75], v[188:191], v[168:171], v[72:75]
	v_mfma_f32_16x16x32_bf16 v[68:71], v[184:187], v[172:175], v[68:71]
	v_mfma_f32_16x16x32_bf16 v[64:67], v[188:191], v[172:175], v[64:67]
	s_waitcnt lgkmcnt(1)
	v_mfma_f32_16x16x32_bf16 v[116:119], v[192:195], v[160:163], v[116:119]
	s_waitcnt lgkmcnt(0)
	v_mfma_f32_16x16x32_bf16 v[104:107], v[196:199], v[160:163], v[104:107]
	v_mfma_f32_16x16x32_bf16 v[100:103], v[192:195], v[164:167], v[100:103]
	v_mfma_f32_16x16x32_bf16 v[88:91], v[196:199], v[164:167], v[88:91]
	v_mfma_f32_16x16x32_bf16 v[84:87], v[192:195], v[176:179], v[84:87]
	v_mfma_f32_16x16x32_bf16 v[72:75], v[196:199], v[176:179], v[72:75]
	v_mfma_f32_16x16x32_bf16 v[68:71], v[192:195], v[180:183], v[68:71]
	v_mfma_f32_16x16x32_bf16 v[64:67], v[196:199], v[180:183], v[64:67]
	s_setprio 0
	s_barrier
	ds_read_b128 v[152:155], v129 offset:49152
	ds_read_b128 v[156:159], v129 offset:51200
	ds_read_b128 v[160:163], v131 offset:49152
	ds_read_b128 v[164:167], v131 offset:51200
	ds_read_b128 v[168:171], v129 offset:53248
	ds_read_b128 v[172:175], v129 offset:55296
	ds_read_b128 v[176:179], v131 offset:53248
	ds_read_b128 v[180:183], v131 offset:55296
	s_lshl_b32 s26, s68, 7
	s_add_u32 s26, s60, s26
	s_addc_u32 s27, s61, 0
	s_mov_b32 s68, m0
	s_mov_b32 m0, s57
	s_nop 2
	global_load_lds_dwordx4 v128, s[26:27]
	s_mov_b32 m0, s68
	s_add_u32 s26, s26, 0x40000
	s_addc_u32 s27, s27, 0
	s_mov_b32 s68, m0
	s_mov_b32 m0, s58
	s_nop 2
	global_load_lds_dwordx4 v128, s[26:27]
	s_mov_b32 m0, s68
	s_barrier
	s_waitcnt lgkmcnt(0)
	s_setprio 1
	s_waitcnt lgkmcnt(7)
	v_mfma_f32_16x16x32_bf16 v[60:63], v[136:139], v[152:155], v[60:63]
	v_mfma_f32_16x16x32_bf16 v[56:59], v[140:143], v[152:155], v[56:59]
	s_waitcnt lgkmcnt(6)
	v_mfma_f32_16x16x32_bf16 v[48:51], v[136:139], v[156:159], v[48:51]
	v_mfma_f32_16x16x32_bf16 v[44:47], v[140:143], v[156:159], v[44:47]
	s_waitcnt lgkmcnt(3)
	v_mfma_f32_16x16x32_bf16 v[32:35], v[136:139], v[168:171], v[32:35]
	v_mfma_f32_16x16x32_bf16 v[28:31], v[140:143], v[168:171], v[28:31]
	s_waitcnt lgkmcnt(2)
	v_mfma_f32_16x16x32_bf16 v[16:19], v[136:139], v[172:175], v[16:19]
	v_mfma_f32_16x16x32_bf16 v[12:15], v[140:143], v[172:175], v[12:15]
	v_mfma_f32_16x16x32_bf16 v[60:63], v[144:147], v[160:163], v[60:63]
	v_mfma_f32_16x16x32_bf16 v[56:59], v[148:151], v[160:163], v[56:59]
	v_mfma_f32_16x16x32_bf16 v[48:51], v[144:147], v[164:167], v[48:51]
	v_mfma_f32_16x16x32_bf16 v[44:47], v[148:151], v[164:167], v[44:47]
	s_waitcnt lgkmcnt(1)
	v_mfma_f32_16x16x32_bf16 v[32:35], v[144:147], v[176:179], v[32:35]
	v_mfma_f32_16x16x32_bf16 v[28:31], v[148:151], v[176:179], v[28:31]
	s_waitcnt lgkmcnt(0)
	v_mfma_f32_16x16x32_bf16 v[16:19], v[144:147], v[180:183], v[16:19]
	v_mfma_f32_16x16x32_bf16 v[12:15], v[148:151], v[180:183], v[12:15]
	s_setprio 0
	s_barrier
	s_add_u32 s68, s69, 0x4000
	s_addc_u32 s69, s72, 0
	s_add_u32 s26, s68, s20
	s_addc_u32 s27, s69, s22
	s_mov_b32 s72, m0
	s_mov_b32 m0, s59
	s_nop 2
	global_load_lds_dwordx4 v134, s[26:27]
	s_mov_b32 m0, s72
	s_add_u32 s26, s68, s21
	s_addc_u32 s27, s69, s28
	s_mov_b32 s68, m0
	s_mov_b32 m0, s70
	s_nop 2
	global_load_lds_dwordx4 v134, s[26:27]
	s_mov_b32 m0, s68
	s_waitcnt vmcnt(10)
	s_barrier
	s_setprio 1
	v_mfma_f32_16x16x32_bf16 v[52:55], v[184:187], v[152:155], v[52:55]
	v_mfma_f32_16x16x32_bf16 v[40:43], v[188:191], v[152:155], v[40:43]
	v_mfma_f32_16x16x32_bf16 v[36:39], v[184:187], v[156:159], v[36:39]
	v_mfma_f32_16x16x32_bf16 v[24:27], v[188:191], v[156:159], v[24:27]
	v_mfma_f32_16x16x32_bf16 v[20:23], v[184:187], v[168:171], v[20:23]
	v_mfma_f32_16x16x32_bf16 v[8:11], v[188:191], v[168:171], v[8:11]
	v_mfma_f32_16x16x32_bf16 v[4:7], v[184:187], v[172:175], v[4:7]
	v_mfma_f32_16x16x32_bf16 v[0:3], v[188:191], v[172:175], v[0:3]
	v_mfma_f32_16x16x32_bf16 v[52:55], v[192:195], v[160:163], v[52:55]
	v_mfma_f32_16x16x32_bf16 v[40:43], v[196:199], v[160:163], v[40:43]
	v_mfma_f32_16x16x32_bf16 v[36:39], v[192:195], v[164:167], v[36:39]
	v_mfma_f32_16x16x32_bf16 v[24:27], v[196:199], v[164:167], v[24:27]
	v_mfma_f32_16x16x32_bf16 v[20:23], v[192:195], v[176:179], v[20:23]
	v_mfma_f32_16x16x32_bf16 v[8:11], v[196:199], v[176:179], v[8:11]
	v_mfma_f32_16x16x32_bf16 v[4:7], v[192:195], v[180:183], v[4:7]
	v_mfma_f32_16x16x32_bf16 v[0:3], v[196:199], v[180:183], v[0:3]
	s_setprio 0
	s_barrier
	s_add_u32 s16, s16, 0x100
	s_addc_u32 s17, s17, 0
	s_cmp_gt_u32 s90, 29
	s_mov_b32 s26, s90
	s_cbranch_scc0 .LBB0_278
	s_waitcnt vmcnt(0)
	s_waitcnt lgkmcnt(0)
	s_mov_b32 s16, s3
	s_cmp_eq_u32 s16, 0
	s_cbranch_scc0 .LBB0_274
	s_barrier
	s_branch .LBB0_274
